# baseline (speedup 1.0000x reference)
.LBB1_37:
	v_or_b32_e32 v12, s6, v1
	v_max_f32_e32 v15, v10, v10
	v_mul_u32_u24_e32 v10, 44, v12
	v_max_f32_e32 v13, v11, v11
	v_max_f32_e32 v14, v9, v9
	v_max_f32_e32 v16, v7, v7
	v_max_f32_e32 v17, v8, v8
	v_max_f32_e32 v18, v6, v6
	v_max_f32_e32 v19, v4, v4
	v_max_f32_e32 v20, v5, v5
	v_max_f32_e32 v21, v2, v2
	v_max_f32_e32 v22, v3, v3
	ds_read2_b32 v[2:3], v10 offset0:6 offset1:7
	ds_read2_b32 v[4:5], v10 offset0:2 offset1:3
	ds_read2_b32 v[6:7], v10 offset0:4 offset1:5
	ds_read2_b32 v[8:9], v10 offset0:8 offset1:9
	ds_read2_b32 v[10:11], v10 offset1:1
	s_waitcnt lgkmcnt(4)
	v_max_f32_e32 v3, v3, v3
	v_max_f32_e32 v2, v2, v2
	s_waitcnt lgkmcnt(3)
	v_max_f32_e32 v5, v5, v5
	s_waitcnt lgkmcnt(1)
	v_max_f32_e32 v9, v9, v9
	v_max_f32_e32 v8, v8, v8
	v_max_f32_e32 v7, v7, v7
	s_waitcnt lgkmcnt(0)
	v_max_f32_e32 v11, v11, v11
	v_max_f32_e32 v4, v4, v4
	v_max_f32_e32 v6, v6, v6
	v_max_f32_e32 v10, v10, v10
	v_min_f32_e32 v3, v13, v3
	v_min_f32_e32 v9, v17, v9
	v_min_f32_e32 v2, v18, v2
	v_min_f32_e32 v8, v22, v8
	v_max_f32_e32 v12, v15, v5
	v_max_f32_e32 v13, v16, v7
	v_max_f32_e32 v17, v20, v4
	v_max_f32_e32 v18, v21, v6
	v_min_f32_e32 v5, v15, v5
	v_min_f32_e32 v7, v16, v7
	v_min_f32_e32 v4, v20, v4
	v_min_f32_e32 v6, v21, v6
	v_max_f32_e32 v15, v14, v3
	v_max_f32_e32 v16, v9, v11
	v_max_f32_e32 v20, v19, v2
	v_max_f32_e32 v21, v8, v10
	v_min_f32_e32 v3, v14, v3
	v_min_f32_e32 v9, v9, v11
	v_min_f32_e32 v2, v19, v2
	v_min_f32_e32 v8, v8, v10
	v_min_f32_e32 v10, v3, v5
	v_min_f32_e32 v11, v7, v9
	v_min_f32_e32 v14, v2, v4
	v_min_f32_e32 v19, v6, v8
	v_max_f32_e32 v3, v3, v5
	v_max_f32_e32 v5, v7, v9
	v_max_f32_e32 v2, v2, v4
	v_max_f32_e32 v4, v6, v8
	v_min_f32_e32 v6, v13, v16
	v_min_f32_e32 v7, v18, v21
	v_min_f32_e32 v8, v10, v11
	v_min_f32_e32 v13, v14, v19
	v_max_f32_e32 v10, v10, v11
	v_max_f32_e32 v11, v14, v19
	v_min_f32_e32 v14, v3, v5
	v_min_f32_e32 v16, v2, v4
	v_max_f32_e32 v3, v3, v5
	v_max_f32_e32 v18, v2, v4
	v_min3_f32 v6, v15, v12, v6
	v_min3_f32 v12, v20, v17, v7
	s_movk_i32 s6, 0x80
	s_and_b64 vcc, exec, s[4:5]
	s_mov_b64 s[4:5], 0
	v_min_f32_e32 v9, v8, v13
	v_max_f32_e32 v4, v8, v13
	v_min_f32_e32 v7, v10, v11
	v_max_f32_e32 v2, v10, v11
	v_min_f32_e32 v10, v14, v16
	v_max_f32_e32 v5, v14, v16
	v_min_f32_e32 v8, v3, v18
	v_max_f32_e32 v3, v3, v18
	v_min_f32_e32 v11, v6, v12
	v_max_f32_e32 v6, v6, v12
	s_cbranch_vccnz .LBB1_37
	v_or_b32_e32 v12, s33, v1
	s_movk_i32 s4, 0x400
	v_cmp_gt_i32_e32 vcc, s4, v12
	s_lshl_b32 s4, s8, 2
	s_add_i32 s4, s4, s76
	s_mul_i32 s4, s4, 12
	v_mov_b32_e32 v13, 0x1e0000
	v_cndmask_b32_e64 v14, 13, 10, vcc
	v_cndmask_b32_e64 v13, v13, 0, vcc
	v_lshlrev_b32_e64 v16, v14, s4
	v_lshlrev_b32_e64 v17, v14, 4
	v_add_u32_e32 v16, v16, v12
	v_lshl_add_u32 v16, v16, 2, v13
	v_mad_u32_u24 v18, v17, 11, v16
	global_store_dword v16, v9, s[70:71]
	v_add_u32_e32 v16, v16, v17
	global_store_dword v16, v4, s[70:71]
	v_add_u32_e32 v16, v16, v17
	global_store_dword v16, v7, s[70:71]
	v_add_u32_e32 v16, v16, v17
	global_store_dword v16, v2, s[70:71]
	v_add_u32_e32 v16, v16, v17
	global_store_dword v16, v10, s[70:71]
	v_add_u32_e32 v16, v16, v17
	global_store_dword v16, v5, s[70:71]
	v_add_u32_e32 v16, v16, v17
	global_store_dword v16, v8, s[70:71]
	v_add_u32_e32 v16, v16, v17
	global_store_dword v16, v3, s[70:71]
	v_add_u32_e32 v16, v16, v17
	global_store_dword v16, v11, s[70:71]
	v_add_u32_e32 v16, v16, v17
	global_store_dword v16, v6, s[70:71]
	global_store_dword v18, v116, s[70:71]
